# as the previous version but the static s_setprio 1 goes to waves 0-3 (the leading half) instead of waves 4-7
# speedup vs baseline: 1.0066x; 1.0066x over previous
.LBB0_118:
	s_ashr_i32 s15, s14, 31
	s_lshl_b64 s[16:17], s[14:15], 20
	s_add_u32 s16, s28, s16
	s_addc_u32 s17, s29, s17
	s_and_b64 s[18:19], s[4:5], exec
	s_cselect_b32 s15, s17, s23
	s_cselect_b32 s75, s16, s22
	s_ashr_i32 s13, s12, 31
	s_lshl_b64 s[18:19], s[12:13], 20
	s_add_u32 s18, s30, s18
	s_addc_u32 s19, s31, s19
	s_and_b64 s[26:27], s[4:5], exec
	s_cselect_b32 s13, s19, s25
	s_cselect_b32 s76, s18, s24
	s_add_u32 s22, s22, 0x80080
	s_addc_u32 s23, s23, 0
	s_add_u32 s77, s24, 0x100
	v_mov_b32_e32 v2, 0
	s_addc_u32 s78, s25, 0
	s_mov_b32 s79, -2
	v_mov_b32_e32 v3, v2
	v_mov_b32_e32 v4, v2
	v_mov_b32_e32 v5, v2
	v_mov_b32_e32 v6, v2
	v_mov_b32_e32 v7, v2
	v_mov_b32_e32 v8, v2
	v_mov_b32_e32 v9, v2
	v_mov_b32_e32 v10, v2
	v_mov_b32_e32 v11, v2
	v_mov_b32_e32 v12, v2
	v_mov_b32_e32 v13, v2
	v_mov_b32_e32 v18, v2
	v_mov_b32_e32 v19, v2
	v_mov_b32_e32 v20, v2
	v_mov_b32_e32 v21, v2
	v_mov_b32_e32 v26, v2
	v_mov_b32_e32 v27, v2
	v_mov_b32_e32 v28, v2
	v_mov_b32_e32 v29, v2
	v_mov_b32_e32 v34, v2
	v_mov_b32_e32 v35, v2
	v_mov_b32_e32 v36, v2
	v_mov_b32_e32 v37, v2
	v_mov_b32_e32 v42, v2
	v_mov_b32_e32 v43, v2
	v_mov_b32_e32 v44, v2
	v_mov_b32_e32 v45, v2
	v_mov_b32_e32 v50, v2
	v_mov_b32_e32 v51, v2
	v_mov_b32_e32 v52, v2
	v_mov_b32_e32 v53, v2
	v_mov_b32_e32 v14, v2
	v_mov_b32_e32 v15, v2
	v_mov_b32_e32 v16, v2
	v_mov_b32_e32 v17, v2
	v_mov_b32_e32 v22, v2
	v_mov_b32_e32 v23, v2
	v_mov_b32_e32 v24, v2
	v_mov_b32_e32 v25, v2
	v_mov_b32_e32 v30, v2
	v_mov_b32_e32 v31, v2
	v_mov_b32_e32 v32, v2
	v_mov_b32_e32 v33, v2
	v_mov_b32_e32 v38, v2
	v_mov_b32_e32 v39, v2
	v_mov_b32_e32 v40, v2
	v_mov_b32_e32 v41, v2
	v_mov_b32_e32 v46, v2
	v_mov_b32_e32 v47, v2
	v_mov_b32_e32 v48, v2
	v_mov_b32_e32 v49, v2
	v_mov_b32_e32 v54, v2
	v_mov_b32_e32 v55, v2
	v_mov_b32_e32 v56, v2
	v_mov_b32_e32 v57, v2
	v_mov_b32_e32 v58, v2
	v_mov_b32_e32 v59, v2
	v_mov_b32_e32 v60, v2
	v_mov_b32_e32 v61, v2
	v_mov_b32_e32 v62, v2
	v_mov_b32_e32 v63, v2
	v_mov_b32_e32 v64, v2
	v_mov_b32_e32 v65, v2
	v_mov_b32_e32 v66, v2
	v_mov_b32_e32 v67, v2
	v_mov_b32_e32 v68, v2
	v_mov_b32_e32 v69, v2
	v_mov_b32_e32 v70, v2
	v_mov_b32_e32 v71, v2
	v_mov_b32_e32 v72, v2
	v_mov_b32_e32 v73, v2
	v_mov_b32_e32 v74, v2
	v_mov_b32_e32 v75, v2
	v_mov_b32_e32 v76, v2
	v_mov_b32_e32 v77, v2
	v_mov_b32_e32 v82, v2
	v_mov_b32_e32 v83, v2
	v_mov_b32_e32 v84, v2
	v_mov_b32_e32 v85, v2
	v_mov_b32_e32 v90, v2
	v_mov_b32_e32 v91, v2
	v_mov_b32_e32 v92, v2
	v_mov_b32_e32 v93, v2
	v_mov_b32_e32 v98, v2
	v_mov_b32_e32 v99, v2
	v_mov_b32_e32 v100, v2
	v_mov_b32_e32 v101, v2
	v_mov_b32_e32 v106, v2
	v_mov_b32_e32 v107, v2
	v_mov_b32_e32 v108, v2
	v_mov_b32_e32 v109, v2
	v_mov_b32_e32 v114, v2
	v_mov_b32_e32 v115, v2
	v_mov_b32_e32 v116, v2
	v_mov_b32_e32 v117, v2
	v_mov_b32_e32 v78, v2
	v_mov_b32_e32 v79, v2
	v_mov_b32_e32 v80, v2
	v_mov_b32_e32 v81, v2
	v_mov_b32_e32 v86, v2
	v_mov_b32_e32 v87, v2
	v_mov_b32_e32 v88, v2
	v_mov_b32_e32 v89, v2
	v_mov_b32_e32 v94, v2
	v_mov_b32_e32 v95, v2
	v_mov_b32_e32 v96, v2
	v_mov_b32_e32 v97, v2
	v_mov_b32_e32 v102, v2
	v_mov_b32_e32 v103, v2
	v_mov_b32_e32 v104, v2
	v_mov_b32_e32 v105, v2
	v_mov_b32_e32 v110, v2
	v_mov_b32_e32 v111, v2
	v_mov_b32_e32 v112, v2
	v_mov_b32_e32 v113, v2
	v_mov_b32_e32 v118, v2
	v_mov_b32_e32 v119, v2
	v_mov_b32_e32 v120, v2
	v_mov_b32_e32 v121, v2
	v_mov_b32_e32 v122, v2
	v_mov_b32_e32 v123, v2
	v_mov_b32_e32 v124, v2
	v_mov_b32_e32 v125, v2
	v_mov_b32_e32 v126, v2
	v_mov_b32_e32 v127, v2
	v_mov_b32_e32 v128, v2
	v_mov_b32_e32 v129, v2
	s_mov_b64 vcc, s[10:11]
	s_cbranch_vccz .Lsp_119
	s_setprio 1

.LBB0_465:
	s_ashr_i32 s27, s26, 31
	s_lshl_b64 s[28:29], s[26:27], 20
	s_add_u32 s28, s23, s28
	s_addc_u32 s29, s33, s29
	s_and_b64 s[30:31], s[12:13], exec
	s_cselect_b32 s1, s29, s37
	s_cselect_b32 s27, s28, s36
	s_ashr_i32 s25, s24, 31
	s_lshl_b64 s[30:31], s[24:25], 20
	s_add_u32 s30, s64, s30
	s_addc_u32 s31, s65, s31
	s_and_b64 s[44:45], s[12:13], exec
	s_cselect_b32 s25, s31, s43
	s_cselect_b32 s35, s30, s42
	s_add_u32 s36, s36, 0x80080
	s_addc_u32 s37, s37, 0
	s_add_u32 s62, s42, 0x100
	v_mov_b32_e32 v2, 0
	s_addc_u32 s63, s43, 0
	s_mov_b32 s83, -2
	v_mov_b32_e32 v3, v2
	v_mov_b32_e32 v4, v2
	v_mov_b32_e32 v5, v2
	v_mov_b32_e32 v6, v2
	v_mov_b32_e32 v7, v2
	v_mov_b32_e32 v8, v2
	v_mov_b32_e32 v9, v2
	v_mov_b32_e32 v18, v2
	v_mov_b32_e32 v19, v2
	v_mov_b32_e32 v20, v2
	v_mov_b32_e32 v21, v2
	v_mov_b32_e32 v22, v2
	v_mov_b32_e32 v23, v2
	v_mov_b32_e32 v24, v2
	v_mov_b32_e32 v25, v2
	v_mov_b32_e32 v34, v2
	v_mov_b32_e32 v35, v2
	v_mov_b32_e32 v36, v2
	v_mov_b32_e32 v37, v2
	v_mov_b32_e32 v38, v2
	v_mov_b32_e32 v39, v2
	v_mov_b32_e32 v40, v2
	v_mov_b32_e32 v41, v2
	v_mov_b32_e32 v50, v2
	v_mov_b32_e32 v51, v2
	v_mov_b32_e32 v52, v2
	v_mov_b32_e32 v53, v2
	v_mov_b32_e32 v54, v2
	v_mov_b32_e32 v55, v2
	v_mov_b32_e32 v56, v2
	v_mov_b32_e32 v57, v2
	v_mov_b32_e32 v10, v2
	v_mov_b32_e32 v11, v2
	v_mov_b32_e32 v12, v2
	v_mov_b32_e32 v13, v2
	s_waitcnt vmcnt(0)
	v_mov_b32_e32 v14, v2
	v_mov_b32_e32 v15, v2
	v_mov_b32_e32 v16, v2
	v_mov_b32_e32 v17, v2
	v_mov_b32_e32 v26, v2
	v_mov_b32_e32 v27, v2
	v_mov_b32_e32 v28, v2
	v_mov_b32_e32 v29, v2
	v_mov_b32_e32 v30, v2
	v_mov_b32_e32 v31, v2
	v_mov_b32_e32 v32, v2
	v_mov_b32_e32 v33, v2
	v_mov_b32_e32 v42, v2
	v_mov_b32_e32 v43, v2
	v_mov_b32_e32 v44, v2
	v_mov_b32_e32 v45, v2
	v_mov_b32_e32 v46, v2
	v_mov_b32_e32 v47, v2
	v_mov_b32_e32 v48, v2
	v_mov_b32_e32 v49, v2
	v_mov_b32_e32 v58, v2
	v_mov_b32_e32 v59, v2
	v_mov_b32_e32 v60, v2
	v_mov_b32_e32 v61, v2
	v_mov_b32_e32 v62, v2
	v_mov_b32_e32 v63, v2
	v_mov_b32_e32 v64, v2
	v_mov_b32_e32 v65, v2
	v_mov_b32_e32 v66, v2
	v_mov_b32_e32 v67, v2
	v_mov_b32_e32 v68, v2
	v_mov_b32_e32 v69, v2
	v_mov_b32_e32 v70, v2
	v_mov_b32_e32 v71, v2
	v_mov_b32_e32 v72, v2
	v_mov_b32_e32 v73, v2
	v_mov_b32_e32 v82, v2
	v_mov_b32_e32 v83, v2
	v_mov_b32_e32 v84, v2
	v_mov_b32_e32 v85, v2
	v_mov_b32_e32 v86, v2
	v_mov_b32_e32 v87, v2
	v_mov_b32_e32 v88, v2
	v_mov_b32_e32 v89, v2
	v_mov_b32_e32 v98, v2
	v_mov_b32_e32 v99, v2
	v_mov_b32_e32 v100, v2
	v_mov_b32_e32 v101, v2
	v_mov_b32_e32 v102, v2
	v_mov_b32_e32 v103, v2
	v_mov_b32_e32 v104, v2
	v_mov_b32_e32 v105, v2
	v_mov_b32_e32 v114, v2
	v_mov_b32_e32 v115, v2
	v_mov_b32_e32 v116, v2
	v_mov_b32_e32 v117, v2
	v_mov_b32_e32 v118, v2
	v_mov_b32_e32 v119, v2
	v_mov_b32_e32 v120, v2
	v_mov_b32_e32 v121, v2
	v_mov_b32_e32 v74, v2
	v_mov_b32_e32 v75, v2
	v_mov_b32_e32 v76, v2
	v_mov_b32_e32 v77, v2
	v_mov_b32_e32 v78, v2
	v_mov_b32_e32 v79, v2
	v_mov_b32_e32 v80, v2
	v_mov_b32_e32 v81, v2
	v_mov_b32_e32 v90, v2
	v_mov_b32_e32 v91, v2
	v_mov_b32_e32 v92, v2
	v_mov_b32_e32 v93, v2
	v_mov_b32_e32 v94, v2
	v_mov_b32_e32 v95, v2
	v_mov_b32_e32 v96, v2
	v_mov_b32_e32 v97, v2
	v_mov_b32_e32 v106, v2
	v_mov_b32_e32 v107, v2
	v_mov_b32_e32 v108, v2
	v_mov_b32_e32 v109, v2
	v_mov_b32_e32 v110, v2
	v_mov_b32_e32 v111, v2
	v_mov_b32_e32 v112, v2
	v_mov_b32_e32 v113, v2
	v_mov_b32_e32 v122, v2
	v_mov_b32_e32 v123, v2
	v_mov_b32_e32 v124, v2
	v_mov_b32_e32 v125, v2
	v_mov_b32_e32 v126, v2
	v_mov_b32_e32 v127, v2
	v_mov_b32_e32 v128, v2
	v_mov_b32_e32 v129, v2
	s_mov_b64 vcc, s[20:21]
	s_cbranch_vccz .Lsp_466
	s_setprio 1

.LBB0_573:
	s_ashr_i32 s15, s14, 31
	s_lshl_b64 s[16:17], s[14:15], 20
	s_add_u32 s16, s28, s16
	s_addc_u32 s17, s29, s17
	s_and_b64 s[18:19], s[4:5], exec
	s_cselect_b32 s15, s17, s23
	s_cselect_b32 s65, s16, s22
	s_ashr_i32 s13, s12, 31
	s_lshl_b64 s[18:19], s[12:13], 20
	s_add_u32 s18, s30, s18
	s_addc_u32 s19, s31, s19
	s_and_b64 s[26:27], s[4:5], exec
	s_cselect_b32 s13, s19, s25
	s_cselect_b32 s66, s18, s24
	s_add_u32 s22, s22, 0x80080
	s_addc_u32 s23, s23, 0
	s_add_u32 s67, s24, 0x100
	v_mov_b32_e32 v2, 0
	s_addc_u32 s68, s25, 0
	s_mov_b32 s69, -2
	v_mov_b32_e32 v3, v2
	v_mov_b32_e32 v4, v2
	v_mov_b32_e32 v5, v2
	v_mov_b32_e32 v6, v2
	v_mov_b32_e32 v7, v2
	v_mov_b32_e32 v8, v2
	v_mov_b32_e32 v9, v2
	v_mov_b32_e32 v18, v2
	v_mov_b32_e32 v19, v2
	v_mov_b32_e32 v20, v2
	v_mov_b32_e32 v21, v2
	v_mov_b32_e32 v22, v2
	v_mov_b32_e32 v23, v2
	v_mov_b32_e32 v24, v2
	v_mov_b32_e32 v25, v2
	v_mov_b32_e32 v34, v2
	v_mov_b32_e32 v35, v2
	v_mov_b32_e32 v36, v2
	v_mov_b32_e32 v37, v2
	v_mov_b32_e32 v38, v2
	v_mov_b32_e32 v39, v2
	v_mov_b32_e32 v40, v2
	v_mov_b32_e32 v41, v2
	v_mov_b32_e32 v50, v2
	v_mov_b32_e32 v51, v2
	v_mov_b32_e32 v52, v2
	v_mov_b32_e32 v53, v2
	v_mov_b32_e32 v54, v2
	v_mov_b32_e32 v55, v2
	v_mov_b32_e32 v56, v2
	v_mov_b32_e32 v57, v2
	v_mov_b32_e32 v10, v2
	v_mov_b32_e32 v11, v2
	v_mov_b32_e32 v12, v2
	v_mov_b32_e32 v13, v2
	v_mov_b32_e32 v14, v2
	v_mov_b32_e32 v15, v2
	v_mov_b32_e32 v16, v2
	v_mov_b32_e32 v17, v2
	v_mov_b32_e32 v26, v2
	v_mov_b32_e32 v27, v2
	v_mov_b32_e32 v28, v2
	v_mov_b32_e32 v29, v2
	v_mov_b32_e32 v30, v2
	v_mov_b32_e32 v31, v2
	v_mov_b32_e32 v32, v2
	v_mov_b32_e32 v33, v2
	v_mov_b32_e32 v42, v2
	v_mov_b32_e32 v43, v2
	v_mov_b32_e32 v44, v2
	v_mov_b32_e32 v45, v2
	v_mov_b32_e32 v46, v2
	v_mov_b32_e32 v47, v2
	v_mov_b32_e32 v48, v2
	v_mov_b32_e32 v49, v2
	v_mov_b32_e32 v58, v2
	v_mov_b32_e32 v59, v2
	v_mov_b32_e32 v60, v2
	v_mov_b32_e32 v61, v2
	v_mov_b32_e32 v62, v2
	v_mov_b32_e32 v63, v2
	v_mov_b32_e32 v64, v2
	v_mov_b32_e32 v65, v2
	v_mov_b32_e32 v66, v2
	v_mov_b32_e32 v67, v2
	v_mov_b32_e32 v68, v2
	v_mov_b32_e32 v69, v2
	v_mov_b32_e32 v70, v2
	v_mov_b32_e32 v71, v2
	v_mov_b32_e32 v72, v2
	v_mov_b32_e32 v73, v2
	v_mov_b32_e32 v82, v2
	v_mov_b32_e32 v83, v2
	v_mov_b32_e32 v84, v2
	v_mov_b32_e32 v85, v2
	v_mov_b32_e32 v86, v2
	v_mov_b32_e32 v87, v2
	v_mov_b32_e32 v88, v2
	v_mov_b32_e32 v89, v2
	v_mov_b32_e32 v98, v2
	v_mov_b32_e32 v99, v2
	v_mov_b32_e32 v100, v2
	v_mov_b32_e32 v101, v2
	v_mov_b32_e32 v102, v2
	v_mov_b32_e32 v103, v2
	v_mov_b32_e32 v104, v2
	v_mov_b32_e32 v105, v2
	v_mov_b32_e32 v114, v2
	v_mov_b32_e32 v115, v2
	v_mov_b32_e32 v116, v2
	v_mov_b32_e32 v117, v2
	v_mov_b32_e32 v118, v2
	v_mov_b32_e32 v119, v2
	v_mov_b32_e32 v120, v2
	v_mov_b32_e32 v121, v2
	v_mov_b32_e32 v74, v2
	v_mov_b32_e32 v75, v2
	v_mov_b32_e32 v76, v2
	v_mov_b32_e32 v77, v2
	v_mov_b32_e32 v78, v2
	v_mov_b32_e32 v79, v2
	v_mov_b32_e32 v80, v2
	v_mov_b32_e32 v81, v2
	v_mov_b32_e32 v90, v2
	v_mov_b32_e32 v91, v2
	v_mov_b32_e32 v92, v2
	v_mov_b32_e32 v93, v2
	v_mov_b32_e32 v94, v2
	v_mov_b32_e32 v95, v2
	v_mov_b32_e32 v96, v2
	v_mov_b32_e32 v97, v2
	v_mov_b32_e32 v106, v2
	v_mov_b32_e32 v107, v2
	v_mov_b32_e32 v108, v2
	v_mov_b32_e32 v109, v2
	v_mov_b32_e32 v110, v2
	v_mov_b32_e32 v111, v2
	v_mov_b32_e32 v112, v2
	v_mov_b32_e32 v113, v2
	v_mov_b32_e32 v122, v2
	v_mov_b32_e32 v123, v2
	v_mov_b32_e32 v124, v2
	v_mov_b32_e32 v125, v2
	v_mov_b32_e32 v126, v2
	v_mov_b32_e32 v127, v2
	v_mov_b32_e32 v128, v2
	v_mov_b32_e32 v129, v2
	s_mov_b64 vcc, s[10:11]
	s_cbranch_vccz .Lsp_574
	s_setprio 1

.LBB0_658:
	s_add_u32 s0, s42, 0x158080
	s_addc_u32 s1, s43, 0
	s_add_u32 s31, s36, 0x100
	v_mov_b32_e32 v2, 0
	s_addc_u32 s35, s37, 0
	s_mov_b32 s44, -2
	v_mov_b32_e32 v3, v2
	v_mov_b32_e32 v4, v2
	v_mov_b32_e32 v5, v2
	v_mov_b32_e32 v6, v2
	v_mov_b32_e32 v7, v2
	v_mov_b32_e32 v8, v2
	v_mov_b32_e32 v9, v2
	v_mov_b32_e32 v18, v2
	v_mov_b32_e32 v19, v2
	v_mov_b32_e32 v20, v2
	v_mov_b32_e32 v21, v2
	v_mov_b32_e32 v22, v2
	v_mov_b32_e32 v23, v2
	v_mov_b32_e32 v24, v2
	v_mov_b32_e32 v25, v2
	v_mov_b32_e32 v34, v2
	v_mov_b32_e32 v35, v2
	v_mov_b32_e32 v36, v2
	v_mov_b32_e32 v37, v2
	v_mov_b32_e32 v38, v2
	v_mov_b32_e32 v39, v2
	v_mov_b32_e32 v40, v2
	v_mov_b32_e32 v41, v2
	v_mov_b32_e32 v50, v2
	v_mov_b32_e32 v51, v2
	v_mov_b32_e32 v52, v2
	v_mov_b32_e32 v53, v2
	v_mov_b32_e32 v54, v2
	v_mov_b32_e32 v55, v2
	v_mov_b32_e32 v56, v2
	v_mov_b32_e32 v57, v2
	v_mov_b32_e32 v10, v2
	v_mov_b32_e32 v11, v2
	v_mov_b32_e32 v12, v2
	v_mov_b32_e32 v13, v2
	v_mov_b32_e32 v14, v2
	v_mov_b32_e32 v15, v2
	v_mov_b32_e32 v16, v2
	v_mov_b32_e32 v17, v2
	v_mov_b32_e32 v26, v2
	v_mov_b32_e32 v27, v2
	v_mov_b32_e32 v28, v2
	v_mov_b32_e32 v29, v2
	v_mov_b32_e32 v30, v2
	v_mov_b32_e32 v31, v2
	v_mov_b32_e32 v32, v2
	v_mov_b32_e32 v33, v2
	v_mov_b32_e32 v42, v2
	v_mov_b32_e32 v43, v2
	v_mov_b32_e32 v44, v2
	v_mov_b32_e32 v45, v2
	v_mov_b32_e32 v46, v2
	v_mov_b32_e32 v47, v2
	v_mov_b32_e32 v48, v2
	v_mov_b32_e32 v49, v2
	v_mov_b32_e32 v58, v2
	v_mov_b32_e32 v59, v2
	v_mov_b32_e32 v60, v2
	v_mov_b32_e32 v61, v2
	v_mov_b32_e32 v62, v2
	v_mov_b32_e32 v63, v2
	v_mov_b32_e32 v64, v2
	v_mov_b32_e32 v65, v2
	v_mov_b32_e32 v66, v2
	v_mov_b32_e32 v67, v2
	v_mov_b32_e32 v68, v2
	v_mov_b32_e32 v69, v2
	v_mov_b32_e32 v70, v2
	v_mov_b32_e32 v71, v2
	v_mov_b32_e32 v72, v2
	v_mov_b32_e32 v73, v2
	v_mov_b32_e32 v82, v2
	v_mov_b32_e32 v83, v2
	v_mov_b32_e32 v84, v2
	v_mov_b32_e32 v85, v2
	v_mov_b32_e32 v86, v2
	v_mov_b32_e32 v87, v2
	v_mov_b32_e32 v88, v2
	v_mov_b32_e32 v89, v2
	v_mov_b32_e32 v98, v2
	v_mov_b32_e32 v99, v2
	v_mov_b32_e32 v100, v2
	v_mov_b32_e32 v101, v2
	v_mov_b32_e32 v102, v2
	v_mov_b32_e32 v103, v2
	v_mov_b32_e32 v104, v2
	v_mov_b32_e32 v105, v2
	v_mov_b32_e32 v114, v2
	v_mov_b32_e32 v115, v2
	v_mov_b32_e32 v116, v2
	v_mov_b32_e32 v117, v2
	v_mov_b32_e32 v118, v2
	v_mov_b32_e32 v119, v2
	v_mov_b32_e32 v120, v2
	v_mov_b32_e32 v121, v2
	v_mov_b32_e32 v74, v2
	v_mov_b32_e32 v75, v2
	v_mov_b32_e32 v76, v2
	v_mov_b32_e32 v77, v2
	v_mov_b32_e32 v78, v2
	v_mov_b32_e32 v79, v2
	v_mov_b32_e32 v80, v2
	v_mov_b32_e32 v81, v2
	v_mov_b32_e32 v90, v2
	v_mov_b32_e32 v91, v2
	v_mov_b32_e32 v92, v2
	v_mov_b32_e32 v93, v2
	v_mov_b32_e32 v94, v2
	v_mov_b32_e32 v95, v2
	v_mov_b32_e32 v96, v2
	v_mov_b32_e32 v97, v2
	v_mov_b32_e32 v106, v2
	v_mov_b32_e32 v107, v2
	v_mov_b32_e32 v108, v2
	v_mov_b32_e32 v109, v2
	v_mov_b32_e32 v110, v2
	v_mov_b32_e32 v111, v2
	v_mov_b32_e32 v112, v2
	v_mov_b32_e32 v113, v2
	v_mov_b32_e32 v122, v2
	v_mov_b32_e32 v123, v2
	v_mov_b32_e32 v124, v2
	v_mov_b32_e32 v125, v2
	v_mov_b32_e32 v126, v2
	v_mov_b32_e32 v127, v2
	v_mov_b32_e32 v128, v2
	v_mov_b32_e32 v129, v2
	s_mov_b64 vcc, s[22:23]
	s_cbranch_vccz .Lsp_659
	s_setprio 1

.LBB0_766:
	s_ashr_i32 s15, s14, 31
	s_lshl_b64 s[16:17], s[14:15], 20
	s_add_u32 s16, s28, s16
	s_addc_u32 s17, s29, s17
	s_and_b64 s[18:19], s[4:5], exec
	s_cselect_b32 s15, s17, s23
	s_cselect_b32 s65, s16, s22
	s_ashr_i32 s13, s12, 31
	s_lshl_b64 s[18:19], s[12:13], 20
	s_add_u32 s18, s30, s18
	s_addc_u32 s19, s31, s19
	s_and_b64 s[26:27], s[4:5], exec
	s_cselect_b32 s13, s19, s25
	s_cselect_b32 s66, s18, s24
	s_add_u32 s22, s22, 0x80080
	s_addc_u32 s23, s23, 0
	s_add_u32 s67, s24, 0x100
	v_mov_b32_e32 v2, 0
	s_addc_u32 s68, s25, 0
	s_mov_b32 s69, -2
	v_mov_b32_e32 v3, v2
	v_mov_b32_e32 v4, v2
	v_mov_b32_e32 v5, v2
	v_mov_b32_e32 v6, v2
	v_mov_b32_e32 v7, v2
	v_mov_b32_e32 v8, v2
	v_mov_b32_e32 v9, v2
	v_mov_b32_e32 v10, v2
	v_mov_b32_e32 v11, v2
	v_mov_b32_e32 v12, v2
	v_mov_b32_e32 v13, v2
	v_mov_b32_e32 v18, v2
	v_mov_b32_e32 v19, v2
	v_mov_b32_e32 v20, v2
	v_mov_b32_e32 v21, v2
	v_mov_b32_e32 v26, v2
	v_mov_b32_e32 v27, v2
	v_mov_b32_e32 v28, v2
	v_mov_b32_e32 v29, v2
	v_mov_b32_e32 v34, v2
	v_mov_b32_e32 v35, v2
	v_mov_b32_e32 v36, v2
	v_mov_b32_e32 v37, v2
	v_mov_b32_e32 v42, v2
	v_mov_b32_e32 v43, v2
	v_mov_b32_e32 v44, v2
	v_mov_b32_e32 v45, v2
	v_mov_b32_e32 v50, v2
	v_mov_b32_e32 v51, v2
	v_mov_b32_e32 v52, v2
	v_mov_b32_e32 v53, v2
	v_mov_b32_e32 v14, v2
	v_mov_b32_e32 v15, v2
	v_mov_b32_e32 v16, v2
	v_mov_b32_e32 v17, v2
	v_mov_b32_e32 v22, v2
	v_mov_b32_e32 v23, v2
	v_mov_b32_e32 v24, v2
	v_mov_b32_e32 v25, v2
	v_mov_b32_e32 v30, v2
	v_mov_b32_e32 v31, v2
	v_mov_b32_e32 v32, v2
	v_mov_b32_e32 v33, v2
	v_mov_b32_e32 v38, v2
	v_mov_b32_e32 v39, v2
	v_mov_b32_e32 v40, v2
	v_mov_b32_e32 v41, v2
	v_mov_b32_e32 v46, v2
	v_mov_b32_e32 v47, v2
	v_mov_b32_e32 v48, v2
	v_mov_b32_e32 v49, v2
	v_mov_b32_e32 v54, v2
	v_mov_b32_e32 v55, v2
	v_mov_b32_e32 v56, v2
	v_mov_b32_e32 v57, v2
	v_mov_b32_e32 v58, v2
	v_mov_b32_e32 v59, v2
	v_mov_b32_e32 v60, v2
	v_mov_b32_e32 v61, v2
	v_mov_b32_e32 v62, v2
	v_mov_b32_e32 v63, v2
	v_mov_b32_e32 v64, v2
	v_mov_b32_e32 v65, v2
	v_mov_b32_e32 v66, v2
	v_mov_b32_e32 v67, v2
	v_mov_b32_e32 v68, v2
	v_mov_b32_e32 v69, v2
	v_mov_b32_e32 v70, v2
	v_mov_b32_e32 v71, v2
	v_mov_b32_e32 v72, v2
	v_mov_b32_e32 v73, v2
	v_mov_b32_e32 v74, v2
	v_mov_b32_e32 v75, v2
	v_mov_b32_e32 v76, v2
	v_mov_b32_e32 v77, v2
	v_mov_b32_e32 v82, v2
	v_mov_b32_e32 v83, v2
	v_mov_b32_e32 v84, v2
	v_mov_b32_e32 v85, v2
	v_mov_b32_e32 v90, v2
	v_mov_b32_e32 v91, v2
	v_mov_b32_e32 v92, v2
	v_mov_b32_e32 v93, v2
	v_mov_b32_e32 v98, v2
	v_mov_b32_e32 v99, v2
	v_mov_b32_e32 v100, v2
	v_mov_b32_e32 v101, v2
	v_mov_b32_e32 v106, v2
	v_mov_b32_e32 v107, v2
	v_mov_b32_e32 v108, v2
	v_mov_b32_e32 v109, v2
	v_mov_b32_e32 v114, v2
	v_mov_b32_e32 v115, v2
	v_mov_b32_e32 v116, v2
	v_mov_b32_e32 v117, v2
	v_mov_b32_e32 v78, v2
	v_mov_b32_e32 v79, v2
	v_mov_b32_e32 v80, v2
	v_mov_b32_e32 v81, v2
	v_mov_b32_e32 v86, v2
	v_mov_b32_e32 v87, v2
	v_mov_b32_e32 v88, v2
	v_mov_b32_e32 v89, v2
	v_mov_b32_e32 v94, v2
	v_mov_b32_e32 v95, v2
	v_mov_b32_e32 v96, v2
	v_mov_b32_e32 v97, v2
	v_mov_b32_e32 v102, v2
	v_mov_b32_e32 v103, v2
	v_mov_b32_e32 v104, v2
	v_mov_b32_e32 v105, v2
	v_mov_b32_e32 v110, v2
	v_mov_b32_e32 v111, v2
	v_mov_b32_e32 v112, v2
	v_mov_b32_e32 v113, v2
	v_mov_b32_e32 v118, v2
	v_mov_b32_e32 v119, v2
	v_mov_b32_e32 v120, v2
	v_mov_b32_e32 v121, v2
	v_mov_b32_e32 v122, v2
	v_mov_b32_e32 v123, v2
	v_mov_b32_e32 v124, v2
	v_mov_b32_e32 v125, v2
	v_mov_b32_e32 v126, v2
	v_mov_b32_e32 v127, v2
	v_mov_b32_e32 v128, v2
	v_mov_b32_e32 v129, v2
	s_mov_b64 vcc, s[10:11]
	s_cbranch_vccz .Lsp_767
	s_setprio 1

.LBB0_1042:
	s_ashr_i32 s35, s34, 31
	s_lshl_b64 s[36:37], s[34:35], 19
	s_add_u32 s36, s29, s36
	s_addc_u32 s37, s33, s37
	s_and_b64 s[38:39], s[12:13], exec
	s_cselect_b32 s1, s37, s49
	s_cselect_b32 s35, s36, s48
	s_ashr_i32 s31, s30, 31
	s_lshl_b64 s[38:39], s[30:31], 19
	s_add_u32 s38, s62, s38
	s_addc_u32 s39, s63, s39
	s_and_b64 s[40:41], s[12:13], exec
	s_cselect_b32 s31, s39, s45
	s_cselect_b32 s43, s38, s44
	s_add_u32 s40, s48, 0x40080
	s_addc_u32 s41, s49, 0
	s_add_u32 s60, s44, 0x100
	v_mov_b32_e32 v34, 0
	s_addc_u32 s61, s45, 0
	s_mov_b32 s81, -2
	v_mov_b32_e32 v35, v34
	v_mov_b32_e32 v36, v34
	v_mov_b32_e32 v37, v34
	v_mov_b32_e32 v38, v34
	v_mov_b32_e32 v39, v34
	v_mov_b32_e32 v40, v34
	v_mov_b32_e32 v41, v34
	v_mov_b32_e32 v50, v34
	v_mov_b32_e32 v51, v34
	v_mov_b32_e32 v52, v34
	v_mov_b32_e32 v53, v34
	v_mov_b32_e32 v54, v34
	v_mov_b32_e32 v55, v34
	v_mov_b32_e32 v56, v34
	v_mov_b32_e32 v57, v34
	v_mov_b32_e32 v66, v34
	v_mov_b32_e32 v67, v34
	v_mov_b32_e32 v68, v34
	v_mov_b32_e32 v69, v34
	v_mov_b32_e32 v70, v34
	v_mov_b32_e32 v71, v34
	v_mov_b32_e32 v72, v34
	v_mov_b32_e32 v73, v34
	v_mov_b32_e32 v82, v34
	v_mov_b32_e32 v83, v34
	v_mov_b32_e32 v84, v34
	v_mov_b32_e32 v85, v34
	v_mov_b32_e32 v86, v34
	v_mov_b32_e32 v87, v34
	v_mov_b32_e32 v88, v34
	v_mov_b32_e32 v89, v34
	v_mov_b32_e32 v42, v34
	v_mov_b32_e32 v43, v34
	v_mov_b32_e32 v44, v34
	v_mov_b32_e32 v45, v34
	v_mov_b32_e32 v46, v34
	v_mov_b32_e32 v47, v34
	v_mov_b32_e32 v48, v34
	v_mov_b32_e32 v49, v34
	v_mov_b32_e32 v58, v34
	v_mov_b32_e32 v59, v34
	v_mov_b32_e32 v60, v34
	v_mov_b32_e32 v61, v34
	v_mov_b32_e32 v62, v34
	v_mov_b32_e32 v63, v34
	v_mov_b32_e32 v64, v34
	v_mov_b32_e32 v65, v34
	v_mov_b32_e32 v74, v34
	v_mov_b32_e32 v75, v34
	v_mov_b32_e32 v76, v34
	v_mov_b32_e32 v77, v34
	v_mov_b32_e32 v78, v34
	v_mov_b32_e32 v79, v34
	v_mov_b32_e32 v80, v34
	v_mov_b32_e32 v81, v34
	v_mov_b32_e32 v90, v34
	v_mov_b32_e32 v91, v34
	v_mov_b32_e32 v92, v34
	v_mov_b32_e32 v93, v34
	v_mov_b32_e32 v94, v34
	v_mov_b32_e32 v95, v34
	v_mov_b32_e32 v96, v34
	v_mov_b32_e32 v97, v34
	v_mov_b32_e32 v98, v34
	v_mov_b32_e32 v99, v34
	v_mov_b32_e32 v100, v34
	v_mov_b32_e32 v101, v34
	v_mov_b32_e32 v102, v34
	v_mov_b32_e32 v103, v34
	v_mov_b32_e32 v104, v34
	v_mov_b32_e32 v105, v34
	v_mov_b32_e32 v114, v34
	v_mov_b32_e32 v115, v34
	v_mov_b32_e32 v116, v34
	v_mov_b32_e32 v117, v34
	v_mov_b32_e32 v118, v34
	v_mov_b32_e32 v119, v34
	v_mov_b32_e32 v120, v34
	v_mov_b32_e32 v121, v34
	v_mov_b32_e32 v130, v34
	v_mov_b32_e32 v131, v34
	v_mov_b32_e32 v132, v34
	v_mov_b32_e32 v133, v34
	v_mov_b32_e32 v134, v34
	v_mov_b32_e32 v135, v34
	v_mov_b32_e32 v136, v34
	v_mov_b32_e32 v137, v34
	v_mov_b32_e32 v146, v34
	v_mov_b32_e32 v147, v34
	v_mov_b32_e32 v148, v34
	v_mov_b32_e32 v149, v34
	v_mov_b32_e32 v150, v34
	v_mov_b32_e32 v151, v34
	v_mov_b32_e32 v152, v34
	v_mov_b32_e32 v153, v34
	v_mov_b32_e32 v106, v34
	v_mov_b32_e32 v107, v34
	v_mov_b32_e32 v108, v34
	v_mov_b32_e32 v109, v34
	v_mov_b32_e32 v110, v34
	v_mov_b32_e32 v111, v34
	v_mov_b32_e32 v112, v34
	v_mov_b32_e32 v113, v34
	v_mov_b32_e32 v122, v34
	v_mov_b32_e32 v123, v34
	v_mov_b32_e32 v124, v34
	v_mov_b32_e32 v125, v34
	v_mov_b32_e32 v126, v34
	v_mov_b32_e32 v127, v34
	v_mov_b32_e32 v128, v34
	v_mov_b32_e32 v129, v34
	v_mov_b32_e32 v138, v34
	v_mov_b32_e32 v139, v34
	v_mov_b32_e32 v140, v34
	v_mov_b32_e32 v141, v34
	v_mov_b32_e32 v142, v34
	v_mov_b32_e32 v143, v34
	v_mov_b32_e32 v144, v34
	v_mov_b32_e32 v145, v34
	v_mov_b32_e32 v154, v34
	v_mov_b32_e32 v155, v34
	v_mov_b32_e32 v156, v34
	v_mov_b32_e32 v157, v34
	v_mov_b32_e32 v158, v34
	v_mov_b32_e32 v159, v34
	v_mov_b32_e32 v160, v34
	v_mov_b32_e32 v161, v34
	s_mov_b64 vcc, s[26:27]
	s_cbranch_vccz .Lsp_1043
	s_setprio 1

.LBB0_1256:
	s_ashr_i32 s11, s10, 31
	s_lshl_b64 s[14:15], s[10:11], 19
	s_add_u32 s14, s29, s14
	s_addc_u32 s15, s30, s15
	s_and_b64 s[16:17], s[24:25], exec
	s_cselect_b32 s11, s15, s21
	s_cselect_b32 s49, s14, s20
	s_ashr_i32 s13, s12, 31
	s_lshl_b64 s[16:17], s[12:13], 19
	s_add_u32 s16, s31, s16
	s_addc_u32 s17, s33, s17
	s_and_b64 s[24:25], s[24:25], exec
	s_cselect_b32 s13, s17, s23
	s_cselect_b32 s60, s16, s22
	s_add_u32 s20, s20, 0x40080
	s_addc_u32 s21, s21, 0
	s_add_u32 s61, s22, 0x100
	v_mov_b32_e32 v30, 0
	s_addc_u32 s62, s23, 0
	s_mov_b32 s63, -2
	v_mov_b32_e32 v31, v30
	v_mov_b32_e32 v32, v30
	v_mov_b32_e32 v33, v30
	v_mov_b32_e32 v34, v30
	v_mov_b32_e32 v35, v30
	v_mov_b32_e32 v36, v30
	v_mov_b32_e32 v37, v30
	v_mov_b32_e32 v46, v30
	v_mov_b32_e32 v47, v30
	v_mov_b32_e32 v48, v30
	v_mov_b32_e32 v49, v30
	v_mov_b32_e32 v50, v30
	v_mov_b32_e32 v51, v30
	v_mov_b32_e32 v52, v30
	v_mov_b32_e32 v53, v30
	v_mov_b32_e32 v62, v30
	v_mov_b32_e32 v63, v30
	v_mov_b32_e32 v64, v30
	v_mov_b32_e32 v65, v30
	v_mov_b32_e32 v66, v30
	v_mov_b32_e32 v67, v30
	v_mov_b32_e32 v68, v30
	v_mov_b32_e32 v69, v30
	v_mov_b32_e32 v78, v30
	v_mov_b32_e32 v79, v30
	v_mov_b32_e32 v80, v30
	v_mov_b32_e32 v81, v30
	v_mov_b32_e32 v82, v30
	v_mov_b32_e32 v83, v30
	v_mov_b32_e32 v84, v30
	v_mov_b32_e32 v85, v30
	v_mov_b32_e32 v26, v30
	v_mov_b32_e32 v27, v30
	v_mov_b32_e32 v28, v30
	v_mov_b32_e32 v29, v30
	v_mov_b32_e32 v38, v30
	v_mov_b32_e32 v39, v30
	v_mov_b32_e32 v40, v30
	v_mov_b32_e32 v41, v30
	v_mov_b32_e32 v42, v30
	v_mov_b32_e32 v43, v30
	v_mov_b32_e32 v44, v30
	v_mov_b32_e32 v45, v30
	v_mov_b32_e32 v54, v30
	v_mov_b32_e32 v55, v30
	v_mov_b32_e32 v56, v30
	v_mov_b32_e32 v57, v30
	v_mov_b32_e32 v58, v30
	v_mov_b32_e32 v59, v30
	v_mov_b32_e32 v60, v30
	v_mov_b32_e32 v61, v30
	v_mov_b32_e32 v70, v30
	v_mov_b32_e32 v71, v30
	v_mov_b32_e32 v72, v30
	v_mov_b32_e32 v73, v30
	v_mov_b32_e32 v74, v30
	v_mov_b32_e32 v75, v30
	v_mov_b32_e32 v76, v30
	v_mov_b32_e32 v77, v30
	v_mov_b32_e32 v86, v30
	v_mov_b32_e32 v87, v30
	v_mov_b32_e32 v88, v30
	v_mov_b32_e32 v89, v30
	v_mov_b32_e32 v94, v30
	v_mov_b32_e32 v95, v30
	v_mov_b32_e32 v96, v30
	v_mov_b32_e32 v97, v30
	v_mov_b32_e32 v98, v30
	v_mov_b32_e32 v99, v30
	v_mov_b32_e32 v100, v30
	v_mov_b32_e32 v101, v30
	v_mov_b32_e32 v110, v30
	v_mov_b32_e32 v111, v30
	v_mov_b32_e32 v112, v30
	v_mov_b32_e32 v113, v30
	v_mov_b32_e32 v114, v30
	v_mov_b32_e32 v115, v30
	v_mov_b32_e32 v116, v30
	v_mov_b32_e32 v117, v30
	v_mov_b32_e32 v126, v30
	v_mov_b32_e32 v127, v30
	v_mov_b32_e32 v128, v30
	v_mov_b32_e32 v129, v30
	v_mov_b32_e32 v130, v30
	v_mov_b32_e32 v131, v30
	v_mov_b32_e32 v132, v30
	v_mov_b32_e32 v133, v30
	v_mov_b32_e32 v142, v30
	v_mov_b32_e32 v143, v30
	v_mov_b32_e32 v144, v30
	v_mov_b32_e32 v145, v30
	v_mov_b32_e32 v146, v30
	v_mov_b32_e32 v147, v30
	v_mov_b32_e32 v148, v30
	v_mov_b32_e32 v149, v30
	v_mov_b32_e32 v90, v30
	v_mov_b32_e32 v91, v30
	v_mov_b32_e32 v92, v30
	v_mov_b32_e32 v93, v30
	v_mov_b32_e32 v102, v30
	v_mov_b32_e32 v103, v30
	v_mov_b32_e32 v104, v30
	v_mov_b32_e32 v105, v30
	v_mov_b32_e32 v106, v30
	v_mov_b32_e32 v107, v30
	v_mov_b32_e32 v108, v30
	v_mov_b32_e32 v109, v30
	v_mov_b32_e32 v118, v30
	v_mov_b32_e32 v119, v30
	v_mov_b32_e32 v120, v30
	v_mov_b32_e32 v121, v30
	v_mov_b32_e32 v122, v30
	v_mov_b32_e32 v123, v30
	v_mov_b32_e32 v124, v30
	v_mov_b32_e32 v125, v30
	v_mov_b32_e32 v134, v30
	v_mov_b32_e32 v135, v30
	v_mov_b32_e32 v136, v30
	v_mov_b32_e32 v137, v30
	v_mov_b32_e32 v138, v30
	v_mov_b32_e32 v139, v30
	v_mov_b32_e32 v140, v30
	v_mov_b32_e32 v141, v30
	v_mov_b32_e32 v150, v30
	v_mov_b32_e32 v151, v30
	v_mov_b32_e32 v152, v30
	v_mov_b32_e32 v153, v30
	s_mov_b64 vcc, s[8:9]
	s_cbranch_vccz .Lsp_1257
	s_setprio 1

.LBB0_1278:
	s_ashr_i32 s11, s10, 31
	s_lshl_b64 s[14:15], s[10:11], 19
	s_add_u32 s14, s29, s14
	s_addc_u32 s15, s30, s15
	s_and_b64 s[18:19], s[16:17], exec
	s_cselect_b32 s11, s15, s23
	s_cselect_b32 s49, s14, s22
	s_ashr_i32 s13, s12, 31
	s_lshl_b64 s[18:19], s[12:13], 19
	s_add_u32 s18, s31, s18
	s_addc_u32 s19, s33, s19
	s_and_b64 s[26:27], s[16:17], exec
	s_cselect_b32 s13, s19, s25
	s_cselect_b32 s50, s18, s24
	s_add_u32 s22, s22, 0x40080
	s_addc_u32 s23, s23, 0
	s_add_u32 s51, s24, 0x100
	v_mov_b32_e32 v30, 0
	s_addc_u32 s60, s25, 0
	s_mov_b32 s61, -2
	v_mov_b32_e32 v31, v30
	v_mov_b32_e32 v32, v30
	v_mov_b32_e32 v33, v30
	v_mov_b32_e32 v34, v30
	v_mov_b32_e32 v35, v30
	v_mov_b32_e32 v36, v30
	v_mov_b32_e32 v37, v30
	v_mov_b32_e32 v46, v30
	v_mov_b32_e32 v47, v30
	v_mov_b32_e32 v48, v30
	v_mov_b32_e32 v49, v30
	v_mov_b32_e32 v50, v30
	v_mov_b32_e32 v51, v30
	v_mov_b32_e32 v52, v30
	v_mov_b32_e32 v53, v30
	v_mov_b32_e32 v62, v30
	v_mov_b32_e32 v63, v30
	v_mov_b32_e32 v64, v30
	v_mov_b32_e32 v65, v30
	v_mov_b32_e32 v66, v30
	v_mov_b32_e32 v67, v30
	v_mov_b32_e32 v68, v30
	v_mov_b32_e32 v69, v30
	v_mov_b32_e32 v78, v30
	v_mov_b32_e32 v79, v30
	v_mov_b32_e32 v80, v30
	v_mov_b32_e32 v81, v30
	v_mov_b32_e32 v82, v30
	v_mov_b32_e32 v83, v30
	v_mov_b32_e32 v84, v30
	v_mov_b32_e32 v85, v30
	v_mov_b32_e32 v26, v30
	v_mov_b32_e32 v27, v30
	v_mov_b32_e32 v28, v30
	v_mov_b32_e32 v29, v30
	v_mov_b32_e32 v38, v30
	v_mov_b32_e32 v39, v30
	v_mov_b32_e32 v40, v30
	v_mov_b32_e32 v41, v30
	v_mov_b32_e32 v42, v30
	v_mov_b32_e32 v43, v30
	v_mov_b32_e32 v44, v30
	v_mov_b32_e32 v45, v30
	v_mov_b32_e32 v54, v30
	v_mov_b32_e32 v55, v30
	v_mov_b32_e32 v56, v30
	v_mov_b32_e32 v57, v30
	v_mov_b32_e32 v58, v30
	v_mov_b32_e32 v59, v30
	v_mov_b32_e32 v60, v30
	v_mov_b32_e32 v61, v30
	v_mov_b32_e32 v70, v30
	v_mov_b32_e32 v71, v30
	v_mov_b32_e32 v72, v30
	v_mov_b32_e32 v73, v30
	v_mov_b32_e32 v74, v30
	v_mov_b32_e32 v75, v30
	v_mov_b32_e32 v76, v30
	v_mov_b32_e32 v77, v30
	v_mov_b32_e32 v86, v30
	v_mov_b32_e32 v87, v30
	v_mov_b32_e32 v88, v30
	v_mov_b32_e32 v89, v30
	v_mov_b32_e32 v94, v30
	v_mov_b32_e32 v95, v30
	v_mov_b32_e32 v96, v30
	v_mov_b32_e32 v97, v30
	v_mov_b32_e32 v98, v30
	v_mov_b32_e32 v99, v30
	v_mov_b32_e32 v100, v30
	v_mov_b32_e32 v101, v30
	v_mov_b32_e32 v110, v30
	v_mov_b32_e32 v111, v30
	v_mov_b32_e32 v112, v30
	v_mov_b32_e32 v113, v30
	v_mov_b32_e32 v114, v30
	v_mov_b32_e32 v115, v30
	v_mov_b32_e32 v116, v30
	v_mov_b32_e32 v117, v30
	v_mov_b32_e32 v126, v30
	v_mov_b32_e32 v127, v30
	v_mov_b32_e32 v128, v30
	v_mov_b32_e32 v129, v30
	v_mov_b32_e32 v130, v30
	v_mov_b32_e32 v131, v30
	v_mov_b32_e32 v132, v30
	v_mov_b32_e32 v133, v30
	v_mov_b32_e32 v142, v30
	v_mov_b32_e32 v143, v30
	v_mov_b32_e32 v144, v30
	v_mov_b32_e32 v145, v30
	v_mov_b32_e32 v146, v30
	v_mov_b32_e32 v147, v30
	v_mov_b32_e32 v148, v30
	v_mov_b32_e32 v149, v30
	v_mov_b32_e32 v90, v30
	v_mov_b32_e32 v91, v30
	v_mov_b32_e32 v92, v30
	v_mov_b32_e32 v93, v30
	v_mov_b32_e32 v102, v30
	v_mov_b32_e32 v103, v30
	v_mov_b32_e32 v104, v30
	v_mov_b32_e32 v105, v30
	v_mov_b32_e32 v106, v30
	v_mov_b32_e32 v107, v30
	v_mov_b32_e32 v108, v30
	v_mov_b32_e32 v109, v30
	v_mov_b32_e32 v118, v30
	v_mov_b32_e32 v119, v30
	v_mov_b32_e32 v120, v30
	v_mov_b32_e32 v121, v30
	v_mov_b32_e32 v122, v30
	v_mov_b32_e32 v123, v30
	v_mov_b32_e32 v124, v30
	v_mov_b32_e32 v125, v30
	v_mov_b32_e32 v134, v30
	v_mov_b32_e32 v135, v30
	v_mov_b32_e32 v136, v30
	v_mov_b32_e32 v137, v30
	v_mov_b32_e32 v138, v30
	v_mov_b32_e32 v139, v30
	v_mov_b32_e32 v140, v30
	v_mov_b32_e32 v141, v30
	v_mov_b32_e32 v150, v30
	v_mov_b32_e32 v151, v30
	v_mov_b32_e32 v152, v30
	v_mov_b32_e32 v153, v30
	s_mov_b64 vcc, s[8:9]
	s_cbranch_vccz .Lsp_1279
	s_setprio 1

.LBB0_1390:
	s_add_u32 s24, s24, 0xe0080
	s_addc_u32 s25, s25, 0
	s_add_u32 s65, s26, 0x100
	v_mov_b32_e32 v32, 0
	s_addc_u32 s66, s27, 0
	s_mov_b32 s67, -2
	v_mov_b32_e32 v33, v32
	v_mov_b32_e32 v34, v32
	v_mov_b32_e32 v35, v32
	v_mov_b32_e32 v36, v32
	v_mov_b32_e32 v37, v32
	v_mov_b32_e32 v38, v32
	v_mov_b32_e32 v39, v32
	v_mov_b32_e32 v48, v32
	v_mov_b32_e32 v49, v32
	v_mov_b32_e32 v50, v32
	v_mov_b32_e32 v51, v32
	v_mov_b32_e32 v52, v32
	v_mov_b32_e32 v53, v32
	v_mov_b32_e32 v54, v32
	v_mov_b32_e32 v55, v32
	v_mov_b32_e32 v64, v32
	v_mov_b32_e32 v65, v32
	v_mov_b32_e32 v66, v32
	v_mov_b32_e32 v67, v32
	v_mov_b32_e32 v68, v32
	v_mov_b32_e32 v69, v32
	v_mov_b32_e32 v70, v32
	v_mov_b32_e32 v71, v32
	v_mov_b32_e32 v80, v32
	v_mov_b32_e32 v81, v32
	v_mov_b32_e32 v82, v32
	v_mov_b32_e32 v83, v32
	v_mov_b32_e32 v84, v32
	v_mov_b32_e32 v85, v32
	v_mov_b32_e32 v86, v32
	v_mov_b32_e32 v87, v32
	v_mov_b32_e32 v40, v32
	v_mov_b32_e32 v41, v32
	v_mov_b32_e32 v42, v32
	v_mov_b32_e32 v43, v32
	v_mov_b32_e32 v44, v32
	v_mov_b32_e32 v45, v32
	v_mov_b32_e32 v46, v32
	v_mov_b32_e32 v47, v32
	v_mov_b32_e32 v56, v32
	v_mov_b32_e32 v57, v32
	v_mov_b32_e32 v58, v32
	v_mov_b32_e32 v59, v32
	v_mov_b32_e32 v60, v32
	v_mov_b32_e32 v61, v32
	v_mov_b32_e32 v62, v32
	v_mov_b32_e32 v63, v32
	v_mov_b32_e32 v72, v32
	v_mov_b32_e32 v73, v32
	v_mov_b32_e32 v74, v32
	v_mov_b32_e32 v75, v32
	v_mov_b32_e32 v76, v32
	v_mov_b32_e32 v77, v32
	v_mov_b32_e32 v78, v32
	v_mov_b32_e32 v79, v32
	v_mov_b32_e32 v88, v32
	v_mov_b32_e32 v89, v32
	v_mov_b32_e32 v90, v32
	v_mov_b32_e32 v91, v32
	v_mov_b32_e32 v92, v32
	v_mov_b32_e32 v93, v32
	v_mov_b32_e32 v94, v32
	v_mov_b32_e32 v95, v32
	v_mov_b32_e32 v96, v32
	v_mov_b32_e32 v97, v32
	v_mov_b32_e32 v98, v32
	v_mov_b32_e32 v99, v32
	v_mov_b32_e32 v100, v32
	v_mov_b32_e32 v101, v32
	v_mov_b32_e32 v102, v32
	v_mov_b32_e32 v103, v32
	v_mov_b32_e32 v112, v32
	v_mov_b32_e32 v113, v32
	v_mov_b32_e32 v114, v32
	v_mov_b32_e32 v115, v32
	v_mov_b32_e32 v116, v32
	v_mov_b32_e32 v117, v32
	v_mov_b32_e32 v118, v32
	v_mov_b32_e32 v119, v32
	v_mov_b32_e32 v128, v32
	v_mov_b32_e32 v129, v32
	v_mov_b32_e32 v130, v32
	v_mov_b32_e32 v131, v32
	v_mov_b32_e32 v132, v32
	v_mov_b32_e32 v133, v32
	v_mov_b32_e32 v134, v32
	v_mov_b32_e32 v135, v32
	v_mov_b32_e32 v144, v32
	v_mov_b32_e32 v145, v32
	v_mov_b32_e32 v146, v32
	v_mov_b32_e32 v147, v32
	v_mov_b32_e32 v148, v32
	v_mov_b32_e32 v149, v32
	v_mov_b32_e32 v150, v32
	v_mov_b32_e32 v151, v32
	v_mov_b32_e32 v104, v32
	v_mov_b32_e32 v105, v32
	v_mov_b32_e32 v106, v32
	v_mov_b32_e32 v107, v32
	v_mov_b32_e32 v108, v32
	v_mov_b32_e32 v109, v32
	v_mov_b32_e32 v110, v32
	v_mov_b32_e32 v111, v32
	v_mov_b32_e32 v120, v32
	v_mov_b32_e32 v121, v32
	v_mov_b32_e32 v122, v32
	v_mov_b32_e32 v123, v32
	v_mov_b32_e32 v124, v32
	v_mov_b32_e32 v125, v32
	v_mov_b32_e32 v126, v32
	v_mov_b32_e32 v127, v32
	v_mov_b32_e32 v136, v32
	v_mov_b32_e32 v137, v32
	v_mov_b32_e32 v138, v32
	v_mov_b32_e32 v139, v32
	v_mov_b32_e32 v140, v32
	v_mov_b32_e32 v141, v32
	v_mov_b32_e32 v142, v32
	v_mov_b32_e32 v143, v32
	v_mov_b32_e32 v152, v32
	v_mov_b32_e32 v153, v32
	v_mov_b32_e32 v154, v32
	v_mov_b32_e32 v155, v32
	v_mov_b32_e32 v156, v32
	v_mov_b32_e32 v157, v32
	v_mov_b32_e32 v158, v32
	v_mov_b32_e32 v159, v32
	s_mov_b64 vcc, s[10:11]
	s_cbranch_vccz .Lsp_1391
	s_setprio 1
